# spatial gating unit: V operand reads of a channel chunk issued together one chunk ahead (plus the attention score-phase variants)
# speedup vs baseline: 1.0146x; 1.0015x over previous
.LBB0_338:
	global_load_dword v181, v[118:119], off
	v_lshl_add_u64 v[190:191], s[92:93], 0, v[116:117]
	global_load_dwordx2 v[66:67], v[190:191], off offset:-128
	global_load_dwordx2 v[68:69], v[190:191], off offset:-64
	global_load_dwordx2 v[138:139], v[190:191], off offset:-32
	global_load_dwordx2 v[136:137], v[190:191], off
	global_load_dwordx2 v[134:135], v[190:191], off offset:32
	global_load_dwordx2 v[132:133], v[190:191], off offset:64
	global_load_dwordx2 v[130:131], v[190:191], off offset:96
	ds_read_b128 v[62:65], v160
	ds_read_b128 v[58:61], v161
	ds_read_b128 v[54:57], v162
	ds_read_b128 v[50:53], v163
	ds_read_b64_tr_b16 v[192:193], v164 offset:32768
	ds_read_b64_tr_b16 v[194:195], v165 offset:33792
	ds_read_b64_tr_b16 v[196:197], v164 offset:40960
	ds_read_b64_tr_b16 v[198:199], v165 offset:41984
	ds_read_b64_tr_b16 v[200:201], v164 offset:49152
	ds_read_b64_tr_b16 v[202:203], v165 offset:50176
	ds_read_b64_tr_b16 v[204:205], v164 offset:57344
	ds_read_b64_tr_b16 v[206:207], v165 offset:58368
	ds_read_b64_tr_b16 v[208:209], v166 offset:32768
	ds_read_b64_tr_b16 v[210:211], v167 offset:33792
	ds_read_b64_tr_b16 v[212:213], v166 offset:40960
	ds_read_b64_tr_b16 v[214:215], v167 offset:41984
	ds_read_b64_tr_b16 v[216:217], v166 offset:49152
	ds_read_b64_tr_b16 v[218:219], v167 offset:50176
	ds_read_b64_tr_b16 v[220:221], v166 offset:57344
	ds_read_b64_tr_b16 v[222:223], v167 offset:58368
	s_add_u32 s74, s74, 0x10000
	s_waitcnt lgkmcnt(8)
	v_mfma_f32_16x16x32_bf16 v[182:185], v[192:195], v[62:65], 0
	s_addc_u32 s75, s75, 0
	s_mov_b64 s[76:77], 0x200
	v_lshl_add_u64 v[124:125], v[124:125], 0, s[4:5]
	v_mfma_f32_16x16x32_bf16 v[182:185], v[196:199], v[58:61], v[182:185]
	v_lshl_add_u64 v[126:127], v[126:127], 0, s[4:5]
	v_lshl_add_u64 v[128:129], v[128:129], 0, s[4:5]
	v_mfma_f32_16x16x32_bf16 v[182:185], v[200:203], v[54:57], v[182:185]
	global_load_dwordx2 v[190:191], v[190:191], off offset:-96
	v_lshl_add_u64 v[108:109], v[108:109], 0, s[4:5]
	v_mfma_f32_16x16x32_bf16 v[182:185], v[204:207], v[50:53], v[182:185]
	v_add_u32_e32 v180, 0x200, v180
	v_lshl_add_u64 v[116:117], v[116:117], 0, s[4:5]
	ds_read_b64_tr_b16 v[192:193], v168 offset:32768
	ds_read_b64_tr_b16 v[194:195], v169 offset:33792
	ds_read_b64_tr_b16 v[196:197], v168 offset:40960
	ds_read_b64_tr_b16 v[198:199], v169 offset:41984
	ds_read_b64_tr_b16 v[200:201], v168 offset:49152
	ds_read_b64_tr_b16 v[202:203], v169 offset:50176
	ds_read_b64_tr_b16 v[204:205], v168 offset:57344
	ds_read_b64_tr_b16 v[206:207], v169 offset:58368
	v_lshl_add_u64 v[118:119], v[118:119], 0, s[76:77]
	s_cmp_lg_u32 s74, 0x40000
	s_waitcnt vmcnt(7)
	v_lshlrev_b32_e32 v186, 16, v66
	v_and_b32_e32 v66, 0xffff0000, v66
	s_nop 0
	v_add_f32_e32 v183, v181, v183
	v_mul_f32_e32 v66, v183, v66
	v_mul_f32_e32 v183, 0x41800000, v66
	v_lshlrev_b32_e32 v66, 16, v67
	v_add_f32_e32 v184, v181, v184
	v_mul_f32_e32 v66, v184, v66
	v_add_f32_e32 v182, v181, v182
	v_mul_f32_e32 v184, 0x41800000, v66
	v_and_b32_e32 v66, 0xffff0000, v67
	v_add_f32_e32 v67, v181, v185
	v_mul_f32_e32 v182, v182, v186
	v_mul_f32_e32 v66, v67, v66
	v_mul_f32_e32 v182, 0x41800000, v182
	v_mul_f32_e32 v67, 0x41800000, v66
	v_cvt_pk_fp8_f32 v66, v182, v183
	v_cvt_pk_fp8_f32 v66, v184, v67 op_sel:[0,0,1]
	s_waitcnt lgkmcnt(8)
	v_mfma_f32_16x16x32_bf16 v[182:185], v[208:211], v[62:65], 0
	s_waitcnt vmcnt(0)
	v_lshlrev_b32_e32 v67, 16, v190
	v_mfma_f32_16x16x32_bf16 v[182:185], v[212:215], v[58:61], v[182:185]
	v_mfma_f32_16x16x32_bf16 v[182:185], v[216:219], v[54:57], v[182:185]
	v_mfma_f32_16x16x32_bf16 v[182:185], v[220:223], v[50:53], v[182:185]
	s_nop 7
	v_add_f32_e32 v182, v181, v182
	ds_read_b64_tr_b16 v[208:209], v170 offset:32768
	ds_read_b64_tr_b16 v[210:211], v171 offset:33792
	ds_read_b64_tr_b16 v[212:213], v170 offset:40960
	ds_read_b64_tr_b16 v[214:215], v171 offset:41984
	ds_read_b64_tr_b16 v[216:217], v170 offset:49152
	ds_read_b64_tr_b16 v[218:219], v171 offset:50176
	ds_read_b64_tr_b16 v[220:221], v170 offset:57344
	ds_read_b64_tr_b16 v[222:223], v171 offset:58368
	v_mul_f32_e32 v67, v182, v67
	v_mul_f32_e32 v182, 0x41800000, v67
	v_and_b32_e32 v67, 0xffff0000, v190
	v_add_f32_e32 v183, v181, v183
	v_mul_f32_e32 v67, v183, v67
	v_mul_f32_e32 v183, 0x41800000, v67
	v_lshlrev_b32_e32 v67, 16, v191
	v_add_f32_e32 v184, v181, v184
	v_mul_f32_e32 v67, v184, v67
	v_mul_f32_e32 v184, 0x41800000, v67
	v_and_b32_e32 v67, 0xffff0000, v191
	v_add_f32_e32 v185, v181, v185
	v_mul_f32_e32 v67, v185, v67
	v_mul_f32_e32 v185, 0x41800000, v67
	v_cvt_pk_fp8_f32 v67, v182, v183
	v_cvt_pk_fp8_f32 v67, v184, v185 op_sel:[0,0,1]
	s_waitcnt lgkmcnt(8)
	v_mfma_f32_16x16x32_bf16 v[182:185], v[192:195], v[62:65], 0
	v_permlane16_swap_b32_e32 v66, v67
	v_mfma_f32_16x16x32_bf16 v[182:185], v[196:199], v[58:61], v[182:185]
	v_mfma_f32_16x16x32_bf16 v[182:185], v[200:203], v[54:57], v[182:185]
	v_mfma_f32_16x16x32_bf16 v[182:185], v[204:207], v[50:53], v[182:185]
	v_lshlrev_b32_e32 v186, 16, v68
	v_and_b32_e32 v68, 0xffff0000, v68
	ds_read_b64_tr_b16 v[192:193], v172 offset:32768
	ds_read_b64_tr_b16 v[194:195], v173 offset:33792
	ds_read_b64_tr_b16 v[196:197], v172 offset:40960
	ds_read_b64_tr_b16 v[198:199], v173 offset:41984
	ds_read_b64_tr_b16 v[200:201], v172 offset:49152
	ds_read_b64_tr_b16 v[202:203], v173 offset:50176
	ds_read_b64_tr_b16 v[204:205], v172 offset:57344
	ds_read_b64_tr_b16 v[206:207], v173 offset:58368
	s_nop 5
	v_add_f32_e32 v183, v181, v183
	v_mul_f32_e32 v68, v183, v68
	v_mul_f32_e32 v183, 0x41800000, v68
	v_lshlrev_b32_e32 v68, 16, v69
	v_add_f32_e32 v184, v181, v184
	v_mul_f32_e32 v68, v184, v68
	v_add_f32_e32 v182, v181, v182
	v_mul_f32_e32 v184, 0x41800000, v68
	v_and_b32_e32 v68, 0xffff0000, v69
	v_add_f32_e32 v69, v181, v185
	v_mul_f32_e32 v182, v182, v186
	v_mul_f32_e32 v68, v69, v68
	v_mul_f32_e32 v182, 0x41800000, v182
	v_mul_f32_e32 v69, 0x41800000, v68
	v_cvt_pk_fp8_f32 v68, v182, v183
	v_cvt_pk_fp8_f32 v68, v184, v69 op_sel:[0,0,1]
	s_waitcnt lgkmcnt(8)
	v_mfma_f32_16x16x32_bf16 v[182:185], v[208:211], v[62:65], 0
	v_mfma_f32_16x16x32_bf16 v[182:185], v[212:215], v[58:61], v[182:185]
	v_mfma_f32_16x16x32_bf16 v[182:185], v[216:219], v[54:57], v[182:185]
	v_mfma_f32_16x16x32_bf16 v[182:185], v[220:223], v[50:53], v[182:185]
	s_nop 7
	v_add_f32_e32 v69, v181, v184
	ds_read_b64_tr_b16 v[208:209], v174 offset:32768
	ds_read_b64_tr_b16 v[210:211], v175 offset:33792
	ds_read_b64_tr_b16 v[212:213], v174 offset:40960
	ds_read_b64_tr_b16 v[214:215], v175 offset:41984
	ds_read_b64_tr_b16 v[216:217], v174 offset:49152
	ds_read_b64_tr_b16 v[218:219], v175 offset:50176
	ds_read_b64_tr_b16 v[220:221], v174 offset:57344
	ds_read_b64_tr_b16 v[222:223], v175 offset:58368
	v_lshlrev_b32_e32 v184, 16, v139
	v_mul_f32_e32 v69, v69, v184
	v_mul_f32_e32 v184, 0x41800000, v69
	v_add_f32_e32 v69, v181, v185
	v_and_b32_e32 v139, 0xffff0000, v139
	v_mul_f32_e32 v69, v69, v139
	v_mul_f32_e32 v139, 0x41800000, v69
	v_add_f32_e32 v69, v181, v182
	v_lshlrev_b32_e32 v182, 16, v138
	v_mul_f32_e32 v69, v69, v182
	v_mul_f32_e32 v182, 0x41800000, v69
	v_add_f32_e32 v69, v181, v183
	v_and_b32_e32 v138, 0xffff0000, v138
	v_mul_f32_e32 v69, v69, v138
	v_mul_f32_e32 v138, 0x41800000, v69
	v_cvt_pk_fp8_f32 v69, v182, v138
	v_cvt_pk_fp8_f32 v69, v184, v139 op_sel:[0,0,1]
	v_lshl_add_u64 v[138:139], s[92:93], 0, v[122:123]
	v_lshl_add_u64 v[122:123], v[122:123], 0, s[96:97]
	v_permlane16_swap_b32_e32 v68, v69
	s_nop 1
	v_permlane32_swap_b32_e32 v66, v68
	v_permlane32_swap_b32_e32 v67, v69
	global_store_dwordx4 v[138:139], v[66:69], off
	s_nop 1
	s_waitcnt lgkmcnt(8)
	v_mfma_f32_16x16x32_bf16 v[66:69], v[192:195], v[62:65], 0
	v_lshlrev_b32_e32 v138, 16, v136
	v_mfma_f32_16x16x32_bf16 v[66:69], v[196:199], v[58:61], v[66:69]
	v_mfma_f32_16x16x32_bf16 v[66:69], v[200:203], v[54:57], v[66:69]
	v_mfma_f32_16x16x32_bf16 v[66:69], v[204:207], v[50:53], v[66:69]
	s_nop 7
	v_add_f32_e32 v66, v181, v66
	ds_read_b64_tr_b16 v[192:193], v176 offset:32768
	ds_read_b64_tr_b16 v[194:195], v177 offset:33792
	ds_read_b64_tr_b16 v[196:197], v176 offset:40960
	ds_read_b64_tr_b16 v[198:199], v177 offset:41984
	ds_read_b64_tr_b16 v[200:201], v176 offset:49152
	ds_read_b64_tr_b16 v[202:203], v177 offset:50176
	ds_read_b64_tr_b16 v[204:205], v176 offset:57344
	ds_read_b64_tr_b16 v[206:207], v177 offset:58368
	v_mul_f32_e32 v66, v66, v138
	v_mul_f32_e32 v138, 0x41800000, v66
	v_and_b32_e32 v66, 0xffff0000, v136
	v_add_f32_e32 v67, v181, v67
	v_mul_f32_e32 v66, v67, v66
	v_mul_f32_e32 v67, 0x41800000, v66
	v_lshlrev_b32_e32 v66, 16, v137
	v_add_f32_e32 v68, v181, v68
	v_mul_f32_e32 v66, v68, v66
	v_mul_f32_e32 v68, 0x41800000, v66
	v_and_b32_e32 v66, 0xffff0000, v137
	v_add_f32_e32 v69, v181, v69
	v_mul_f32_e32 v66, v69, v66
	v_mul_f32_e32 v69, 0x41800000, v66
	v_cvt_pk_fp8_f32 v66, v138, v67
	s_waitcnt lgkmcnt(8)
	v_mfma_f32_16x16x32_bf16 v[136:139], v[208:211], v[62:65], 0
	v_cvt_pk_fp8_f32 v66, v68, v69 op_sel:[0,0,1]
	v_lshlrev_b32_e32 v67, 16, v134
	v_mfma_f32_16x16x32_bf16 v[136:139], v[212:215], v[58:61], v[136:139]
	v_mfma_f32_16x16x32_bf16 v[136:139], v[216:219], v[54:57], v[136:139]
	v_mfma_f32_16x16x32_bf16 v[136:139], v[220:223], v[50:53], v[136:139]
	s_nop 7
	v_add_f32_e32 v68, v181, v136
	ds_read_b64_tr_b16 v[208:209], v178 offset:32768
	ds_read_b64_tr_b16 v[210:211], v179 offset:33792
	ds_read_b64_tr_b16 v[212:213], v178 offset:40960
	ds_read_b64_tr_b16 v[214:215], v179 offset:41984
	ds_read_b64_tr_b16 v[216:217], v178 offset:49152
	ds_read_b64_tr_b16 v[218:219], v179 offset:50176
	ds_read_b64_tr_b16 v[220:221], v178 offset:57344
	ds_read_b64_tr_b16 v[222:223], v179 offset:58368
	v_mul_f32_e32 v67, v68, v67
	v_mul_f32_e32 v68, 0x41800000, v67
	v_and_b32_e32 v67, 0xffff0000, v134
	v_add_f32_e32 v69, v181, v137
	v_mul_f32_e32 v67, v69, v67
	v_mul_f32_e32 v69, 0x41800000, v67
	v_lshlrev_b32_e32 v67, 16, v135
	v_add_f32_e32 v134, v181, v138
	v_mul_f32_e32 v67, v134, v67
	v_mul_f32_e32 v134, 0x41800000, v67
	v_and_b32_e32 v67, 0xffff0000, v135
	v_add_f32_e32 v135, v181, v139
	v_mul_f32_e32 v67, v135, v67
	v_mul_f32_e32 v135, 0x41800000, v67
	v_cvt_pk_fp8_f32 v67, v68, v69
	v_lshlrev_b32_e32 v68, 16, v132
	v_cvt_pk_fp8_f32 v67, v134, v135 op_sel:[0,0,1]
	s_waitcnt lgkmcnt(8)
	v_mfma_f32_16x16x32_bf16 v[134:137], v[192:195], v[62:65], 0
	v_permlane16_swap_b32_e32 v66, v67
	v_mfma_f32_16x16x32_bf16 v[134:137], v[196:199], v[58:61], v[134:137]
	v_mfma_f32_16x16x32_bf16 v[134:137], v[200:203], v[54:57], v[134:137]
	v_mfma_f32_16x16x32_bf16 v[134:137], v[204:207], v[50:53], v[134:137]
	s_nop 7
	v_add_f32_e32 v69, v181, v134
	v_mul_f32_e32 v68, v69, v68
	v_mul_f32_e32 v69, 0x41800000, v68
	v_and_b32_e32 v68, 0xffff0000, v132
	v_add_f32_e32 v132, v181, v135
	v_mul_f32_e32 v68, v132, v68
	v_mul_f32_e32 v132, 0x41800000, v68
	v_lshlrev_b32_e32 v68, 16, v133
	v_add_f32_e32 v134, v181, v136
	v_mul_f32_e32 v68, v134, v68
	v_mul_f32_e32 v134, 0x41800000, v68
	v_and_b32_e32 v68, 0xffff0000, v133
	v_add_f32_e32 v133, v181, v137
	v_mul_f32_e32 v68, v133, v68
	v_mul_f32_e32 v133, 0x41800000, v68
	v_cvt_pk_fp8_f32 v68, v69, v132
	v_cvt_pk_fp8_f32 v68, v134, v133 op_sel:[0,0,1]
	s_waitcnt lgkmcnt(0)
	v_mfma_f32_16x16x32_bf16 v[62:65], v[208:211], v[62:65], 0
	v_mfma_f32_16x16x32_bf16 v[58:61], v[212:215], v[58:61], v[62:65]
	s_nop 3
	v_mfma_f32_16x16x32_bf16 v[54:57], v[216:219], v[54:57], v[58:61]
	s_nop 2
	v_mfma_f32_16x16x32_bf16 v[50:53], v[220:223], v[50:53], v[54:57]
	s_nop 2
	v_lshlrev_b32_e32 v54, 16, v131
	s_nop 3
	v_add_f32_e32 v52, v181, v52
	v_mul_f32_e32 v52, v52, v54
	v_add_f32_e32 v53, v181, v53
	v_and_b32_e32 v54, 0xffff0000, v131
	v_mul_f32_e32 v53, v53, v54
	v_add_f32_e32 v50, v181, v50
	v_lshlrev_b32_e32 v54, 16, v130
	v_mul_f32_e32 v50, v50, v54
	v_add_f32_e32 v51, v181, v51
	v_and_b32_e32 v54, 0xffff0000, v130
	v_mul_f32_e32 v51, v51, v54
	v_mul_f32_e32 v50, 0x41800000, v50
	v_mul_f32_e32 v51, 0x41800000, v51
	v_cvt_pk_fp8_f32 v69, v50, v51
	v_mul_f32_e32 v52, 0x41800000, v52
	v_mul_f32_e32 v53, 0x41800000, v53
	v_lshl_add_u64 v[50:51], s[92:93], 0, v[120:121]
	v_cvt_pk_fp8_f32 v69, v52, v53 op_sel:[0,0,1]
	v_lshl_add_u64 v[120:121], v[120:121], 0, s[96:97]
	s_nop 0
	v_permlane16_swap_b32_e32 v68, v69
	s_nop 1
	v_permlane32_swap_b32_e32 v66, v68
	v_permlane32_swap_b32_e32 v67, v69
	global_store_dwordx4 v[50:51], v[66:69], off
	s_barrier
	s_cbranch_scc0 .LBB0_330
